# MLA softmax: cross-lane max exchange moved into the rare rescale path; register copies before the K/V tile loads removed
# speedup vs baseline: 1.0215x; 1.0021x over previous
.LBB0_458:
	s_add_i32 s46, s47, 1
	s_cmp_lt_u32 s46, s43
	s_cselect_b64 s[26:27], -1, 0
	s_cmp_ge_u32 s46, s43
	s_cbranch_scc1 .LBB0_460
	s_add_u32 s48, s78, s20
	s_addc_u32 s49, s79, s21
	global_load_dwordx4 v[134:137], v1, s[48:49]
	global_load_dwordx4 v[138:141], v173, s[48:49]
	s_add_u32 s48, s78, s22
	s_addc_u32 s49, s79, s23
	global_load_dwordx4 v[142:145], v177, s[48:49]
	s_add_u32 s48, s78, s24
	s_addc_u32 s49, s79, s25
	global_load_dwordx4 v[154:157], v178, s[48:49]
	global_load_dwordx4 v[158:161], v179, s[48:49]

.LBB0_463:
	s_nop 9
	v_max3_f32 v206, v82, v66, s90
	v_max_f32_e32 v208, v83, v67
	v_max3_f32 v206, v206, v84, v68
	v_max3_f32 v208, v208, v85, v69
	v_max3_f32 v206, v206, v86, v70
	v_max3_f32 v208, v208, v87, v71
	v_max3_f32 v206, v206, v88, v72
	v_max3_f32 v208, v208, v89, v73
	v_max3_f32 v206, v206, v90, v74
	v_max3_f32 v208, v208, v91, v75
	v_max3_f32 v206, v206, v92, v76
	v_max3_f32 v208, v208, v93, v77
	v_max3_f32 v206, v206, v94, v78
	v_max3_f32 v208, v208, v95, v79
	v_max3_f32 v206, v206, v96, v80
	v_max3_f32 v208, v208, v97, v81
	v_max_f32_e32 v206, v206, v208
	v_add_f32_e32 v208, 0x4299999a, v207
	v_cmp_gt_f32_e32 vcc, v206, v208
	s_cbranch_vccnz .Lmy_lazy_a
	v_mov_b32_e32 v206, v207
	s_branch .LBB0_465
.Lmy_lazy_a:
	ds_bpermute_b32 v208, v236, v206
	s_waitcnt lgkmcnt(0)
	v_max3_f32 v206, v207, v206, v208
	v_sub_f32_e32 v207, v207, v206
	v_mul_f32_e32 v207, 0x3dd53b94, v207
	v_exp_f32_e32 v208, v207
	s_nop 0
	v_pk_mul_f32 v[64:65], v[64:65], v[208:209] op_sel_hi:[1,0]
	v_pk_mul_f32 v[62:63], v[62:63], v[208:209] op_sel_hi:[1,0]
	v_pk_mul_f32 v[60:61], v[60:61], v[208:209] op_sel_hi:[1,0]
	v_pk_mul_f32 v[58:59], v[58:59], v[208:209] op_sel_hi:[1,0]
	v_pk_mul_f32 v[56:57], v[56:57], v[208:209] op_sel_hi:[1,0]
	v_pk_mul_f32 v[54:55], v[54:55], v[208:209] op_sel_hi:[1,0]
	v_pk_mul_f32 v[52:53], v[52:53], v[208:209] op_sel_hi:[1,0]
	v_pk_mul_f32 v[50:51], v[50:51], v[208:209] op_sel_hi:[1,0]
	v_pk_mul_f32 v[48:49], v[48:49], v[208:209] op_sel_hi:[1,0]
	v_pk_mul_f32 v[46:47], v[46:47], v[208:209] op_sel_hi:[1,0]
	v_pk_mul_f32 v[44:45], v[44:45], v[208:209] op_sel_hi:[1,0]
	v_pk_mul_f32 v[42:43], v[42:43], v[208:209] op_sel_hi:[1,0]
	v_pk_mul_f32 v[40:41], v[40:41], v[208:209] op_sel_hi:[1,0]
	v_pk_mul_f32 v[38:39], v[38:39], v[208:209] op_sel_hi:[1,0]
	v_pk_mul_f32 v[36:37], v[36:37], v[208:209] op_sel_hi:[1,0]
	v_pk_mul_f32 v[34:35], v[34:35], v[208:209] op_sel_hi:[1,0]
	v_pk_mul_f32 v[32:33], v[32:33], v[208:209] op_sel_hi:[1,0]
	v_pk_mul_f32 v[30:31], v[30:31], v[208:209] op_sel_hi:[1,0]
	v_pk_mul_f32 v[28:29], v[28:29], v[208:209] op_sel_hi:[1,0]
	v_pk_mul_f32 v[26:27], v[26:27], v[208:209] op_sel_hi:[1,0]
	v_pk_mul_f32 v[24:25], v[24:25], v[208:209] op_sel_hi:[1,0]
	v_pk_mul_f32 v[22:23], v[22:23], v[208:209] op_sel_hi:[1,0]
	v_pk_mul_f32 v[20:21], v[20:21], v[208:209] op_sel_hi:[1,0]
	v_pk_mul_f32 v[18:19], v[18:19], v[208:209] op_sel_hi:[1,0]
	v_pk_mul_f32 v[16:17], v[16:17], v[208:209] op_sel_hi:[1,0]
	v_pk_mul_f32 v[14:15], v[14:15], v[208:209] op_sel_hi:[1,0]
	v_pk_mul_f32 v[12:13], v[12:13], v[208:209] op_sel_hi:[1,0]
	v_pk_mul_f32 v[10:11], v[10:11], v[208:209] op_sel_hi:[1,0]
	v_pk_mul_f32 v[8:9], v[8:9], v[208:209] op_sel_hi:[1,0]
	v_pk_mul_f32 v[6:7], v[6:7], v[208:209] op_sel_hi:[1,0]
	v_pk_mul_f32 v[4:5], v[4:5], v[208:209] op_sel_hi:[1,0]
	v_pk_mul_f32 v[2:3], v[2:3], v[208:209] op_sel_hi:[1,0]
	v_mul_f32_e32 v205, v205, v208

.LBB0_471:
	s_cmp_lt_u32 s21, s14
	s_cselect_b64 s[12:13], -1, 0
	s_cmp_ge_u32 s21, s14
	s_cselect_b64 s[10:11], -1, 0
	s_and_b64 vcc, exec, s[10:11]
	s_cbranch_vccnz .LBB0_473
	s_add_u32 s22, s78, s8
	s_addc_u32 s23, s79, s9
	global_load_dwordx4 v[134:137], v173, s[22:23]
	global_load_dwordx4 v[138:141], v176, s[22:23]
	s_add_u32 s22, s78, s6
	s_addc_u32 s23, s79, s7
	global_load_dwordx4 v[142:145], v178, s[22:23]
	s_add_u32 s22, s78, s4
	s_addc_u32 s23, s79, s5
	global_load_dwordx4 v[154:157], v179, s[22:23]
	global_load_dwordx4 v[158:161], v180, s[22:23]

.LBB0_476:
	s_nop 9
	v_max3_f32 v207, v82, v66, s90
	v_max_f32_e32 v209, v83, v67
	v_max3_f32 v207, v207, v84, v68
	v_max3_f32 v209, v209, v85, v69
	v_max3_f32 v207, v207, v86, v70
	v_max3_f32 v209, v209, v87, v71
	v_max3_f32 v207, v207, v88, v72
	v_max3_f32 v209, v209, v89, v73
	v_max3_f32 v207, v207, v90, v74
	v_max3_f32 v209, v209, v91, v75
	v_max3_f32 v207, v207, v92, v76
	v_max3_f32 v209, v209, v93, v77
	v_max3_f32 v207, v207, v94, v78
	v_max3_f32 v209, v209, v95, v79
	v_max3_f32 v207, v207, v96, v80
	v_max3_f32 v209, v209, v97, v81
	v_max_f32_e32 v207, v207, v209
	v_add_f32_e32 v209, 0x4299999a, v208
	v_cmp_gt_f32_e32 vcc, v207, v209
	s_cbranch_vccnz .Lmy_lazy_b
	v_mov_b32_e32 v207, v208
	s_branch .LBB0_478
.Lmy_lazy_b:
	ds_bpermute_b32 v209, v1, v207
	s_waitcnt lgkmcnt(0)
	v_max3_f32 v207, v208, v207, v209
	v_sub_f32_e32 v208, v208, v207
	v_mul_f32_e32 v208, 0x3dd53b94, v208
	v_exp_f32_e32 v208, v208
	s_nop 0
	v_pk_mul_f32 v[64:65], v[64:65], v[208:209] op_sel_hi:[1,0]
	v_pk_mul_f32 v[62:63], v[62:63], v[208:209] op_sel_hi:[1,0]
	v_pk_mul_f32 v[60:61], v[60:61], v[208:209] op_sel_hi:[1,0]
	v_pk_mul_f32 v[58:59], v[58:59], v[208:209] op_sel_hi:[1,0]
	v_pk_mul_f32 v[56:57], v[56:57], v[208:209] op_sel_hi:[1,0]
	v_pk_mul_f32 v[54:55], v[54:55], v[208:209] op_sel_hi:[1,0]
	v_pk_mul_f32 v[52:53], v[52:53], v[208:209] op_sel_hi:[1,0]
	v_pk_mul_f32 v[50:51], v[50:51], v[208:209] op_sel_hi:[1,0]
	v_pk_mul_f32 v[48:49], v[48:49], v[208:209] op_sel_hi:[1,0]
	v_pk_mul_f32 v[46:47], v[46:47], v[208:209] op_sel_hi:[1,0]
	v_pk_mul_f32 v[44:45], v[44:45], v[208:209] op_sel_hi:[1,0]
	v_pk_mul_f32 v[42:43], v[42:43], v[208:209] op_sel_hi:[1,0]
	v_pk_mul_f32 v[40:41], v[40:41], v[208:209] op_sel_hi:[1,0]
	v_pk_mul_f32 v[38:39], v[38:39], v[208:209] op_sel_hi:[1,0]
	v_pk_mul_f32 v[36:37], v[36:37], v[208:209] op_sel_hi:[1,0]
	v_pk_mul_f32 v[34:35], v[34:35], v[208:209] op_sel_hi:[1,0]
	v_pk_mul_f32 v[32:33], v[32:33], v[208:209] op_sel_hi:[1,0]
	v_pk_mul_f32 v[30:31], v[30:31], v[208:209] op_sel_hi:[1,0]
	v_pk_mul_f32 v[28:29], v[28:29], v[208:209] op_sel_hi:[1,0]
	v_pk_mul_f32 v[26:27], v[26:27], v[208:209] op_sel_hi:[1,0]
	v_pk_mul_f32 v[24:25], v[24:25], v[208:209] op_sel_hi:[1,0]
	v_pk_mul_f32 v[22:23], v[22:23], v[208:209] op_sel_hi:[1,0]
	v_pk_mul_f32 v[20:21], v[20:21], v[208:209] op_sel_hi:[1,0]
	v_pk_mul_f32 v[18:19], v[18:19], v[208:209] op_sel_hi:[1,0]
	v_pk_mul_f32 v[16:17], v[16:17], v[208:209] op_sel_hi:[1,0]
	v_pk_mul_f32 v[14:15], v[14:15], v[208:209] op_sel_hi:[1,0]
	v_pk_mul_f32 v[12:13], v[12:13], v[208:209] op_sel_hi:[1,0]
	v_pk_mul_f32 v[10:11], v[10:11], v[208:209] op_sel_hi:[1,0]
	v_pk_mul_f32 v[8:9], v[8:9], v[208:209] op_sel_hi:[1,0]
	v_pk_mul_f32 v[6:7], v[6:7], v[208:209] op_sel_hi:[1,0]
	v_pk_mul_f32 v[4:5], v[4:5], v[208:209] op_sel_hi:[1,0]
	v_pk_mul_f32 v[2:3], v[2:3], v[208:209] op_sel_hi:[1,0]
	v_mul_f32_e32 v205, v205, v208
